# placement: expert GEMM loops at offset 44 mod 64 (60 more pad bytes ahead of the gate/up GEMM)
# baseline (speedup 1.0000x reference)
;     __device__ __forceinline__ bool next(int i, Unit& u) const { if (!order_tile(i, G, c, nM, nN, u.pm, u.pn)) return false; u.A = A0 + (size_t)u.pm * tstep; u.B = B0 + (size_t)u.pn * tstep; return true; }
;     __device__ __forceinline__ bool next(int i, Unit& u) const { if (!order_tile(i, G, c, nM, nN, u.pm, u.pn)) return false; u.A = A0 + (size_t)(u.pn >> 1) * groupA + (size_t)u.pm * tstep; u.B = B0 + (size_t)u.pn * tstep; return true; }
; #define PG8_STAGE(bufoff, gbase, voff) do { _Pragma("unroll") for (int _i = 0; _i < 2; ++_i) glds16_s((const void*)((const char*)(gbase) + _i * r64), (voff), ldsb + (unsigned)(bufoff) + ldsw + _i * 8192u); } while (0)
; #define PG8_WAIT_V(n) asm volatile("s_waitcnt vmcnt(" #n ")" ::: "memory")
; #define PG8_BAR __builtin_amdgcn_s_barrier()
; template <class Epi, class Sched, bool FP8 = false>
; __device__ __forceinline__ void gemm_phase(LAS unsigned char* lds, const int Kb, const int nt  , const Sched& S, const Epi& E) {
;     ...
;     { int R, C; stage_rc(tid * 16, R, C); const int Rb = Epi::PERM ? ((R & ~31) + perm32(R & 31)) : R;
;         voffA = (unsigned)(R * Kb + C * 2); voffB = (unsigned)(Rb * Kb + C * 2); }
;     const size_t r64 = (size_t)64 * Kb;
;     const size_t kstep = (size_t)(BK * 2);
;     const size_t hstep = (size_t)HALF * Kb;
;     const unsigned ldsw = (unsigned)wid * 1024u, ldsb = (unsigned)(uintptr_t)lds;
;     const int aoff = lds_byte(wr * 64 + fr, fq * 8), boff = lds_byte(wc * 32 + fr, fq * 8);
;     ...
;     Unit cur, nxt; int ui = 0;
;     if (!S.next(0, cur)) return;
;     f32x4 acc[2][2][4][2];
; #pragma unroll
;     for (int a = 0; a < 2; ++a)
; #pragma unroll
;         for (int b = 0; b < 2; ++b)
; #pragma unroll
;             for (int m = 0; m < 4; ++m)
; #pragma unroll
;                 for (int n = 0; n < 2; ++n) acc[a][b][m][n] = (f32x4){0.f, 0.f, 0.f, 0.f};
;     bf16x8 At[4][2], B0[2][2], B1[2][2]; i32x8 A8[4], B08[2], B18[2];
;     const char* cA = cur.A; const char* cB = cur.B;
;     PG8_STAGE(PG8_SB(0, 0), cB, voffB); PG8_STAGE(PG8_SA(0, 0), cA, voffA); PG8_STAGE(PG8_SB(0, 1), cB + hstep, voffB); PG8_STAGE(PG8_SA(0, 1), cA + hstep, voffA);
;     if (wr == 1) PG8_BAR;
;     PG8_WAIT_V(4); PG8_BAR;
;     PG8_STAGE(PG8_SB(1, 0), cB + kstep, voffB); PG8_STAGE(PG8_SA(1, 0), cA + kstep, voffA); PG8_STAGE(PG8_SB(1, 1), cB + hstep + kstep, voffB);
;     PG8_WAIT_V(6); PG8_BAR;
.LBB0_2748:
	v_readlane_b32 s2, v241, 5
	v_readlane_b32 s3, v241, 6
	s_add_u32 s2, s2, 0x31500000
	s_addc_u32 s3, s3, 0
	s_lshl_b32 s6, s6, 5
	s_and_b32 s55, s6, 0x60
	s_lshl_b32 s54, s7, 6
	s_lshl_b32 s8, s7, 13
	s_lshl_b32 s9, s55, 7
	s_add_u32 s6, s24, 0x80
	s_addc_u32 s7, s25, 0
	s_add_i32 s57, s19, 0x18000
	s_waitcnt vmcnt(4)
	s_barrier
	s_mov_b32 s10, m0
	s_mov_b32 m0, s57
	s_nop 0
	global_load_lds_dwordx4 v138, s[6:7]
	s_mov_b32 m0, s10
	s_add_u32 s6, s24, 0x20080
	s_addc_u32 s7, s25, 0
	s_add_i32 s58, s19, 0x1a000
	s_mov_b32 s10, m0
	s_mov_b32 m0, s58
	s_nop 0
	global_load_lds_dwordx4 v138, s[6:7]
	s_mov_b32 m0, s10
	s_add_u32 s6, s22, 0x80
	s_addc_u32 s7, s23, 0
	s_add_i32 s59, s19, 0x8000
	s_mov_b32 s10, m0
	s_mov_b32 m0, s59
	s_nop 0
	global_load_lds_dwordx4 v1, s[6:7]
	s_mov_b32 m0, s10
	s_add_u32 s6, s22, 0x20080
	s_addc_u32 s7, s23, 0
	s_add_i32 s60, s19, 0xa000
	s_mov_b32 s10, m0
	s_mov_b32 m0, s60
	s_nop 0
	global_load_lds_dwordx4 v1, s[6:7]
	s_mov_b32 m0, s10
	s_add_u32 s6, s24, 0x40080
	s_addc_u32 s7, s25, 0
	s_add_i32 s61, s19, 0x1c000
	v_lshlrev_b32_e32 v3, 6, v0
	v_lshlrev_b32_e32 v4, 2, v0
	s_mov_b32 s10, m0
	s_mov_b32 m0, s61
	s_nop 0
	global_load_lds_dwordx4 v138, s[6:7]
	s_mov_b32 m0, s10
	s_add_u32 s6, s24, 0x60080
	v_and_b32_e32 v2, 48, v0
	v_and_b32_e32 v3, 0x3c0, v3
	v_and_b32_e32 v4, 32, v4
	s_addc_u32 s7, s25, 0
	s_add_i32 s62, s19, 0x1e000
	s_mov_b32 s10, m0
	s_mov_b32 m0, s62
	s_nop 0
	global_load_lds_dwordx4 v138, s[6:7]
	s_mov_b32 m0, s10
	v_bitop3_b32 v2, v3, v4, v2 bitop3:0x36
	s_waitcnt vmcnt(6)
	s_add_i32 s6, s9, 0
	v_add_u32_e32 v3, s6, v2
	v_add_u32_e32 v2, 0, v2
	s_mov_b32 s6, 0x39000000
	s_mov_b32 s56, 0
	s_add_i32 s63, s19, 0xc000
	v_add_u32_e32 v139, 0x10000, v3
	v_add_u32_e32 v140, 0x10400, v3
	v_add_u32_e32 v141, 0x10800, v3
	v_add_u32_e32 v142, 0x10c00, v3
	s_add_i32 s64, s19, 0xe000
	v_add_u32_e32 v143, 0x14000, v3
	v_add_u32_e32 v144, 0x14400, v3
	v_add_u32_e32 v145, 0x14800, v3
	v_add_u32_e32 v146, 0x14c00, v3
	v_add_u32_e32 v147, 0x18000, v3
	v_add_u32_e32 v148, 0x18400, v3
	v_add_u32_e32 v149, 0x18800, v3
	v_add_u32_e32 v150, 0x18c00, v3
	v_add_u32_e32 v151, 0x1c000, v3
	v_add_u32_e32 v152, 0x1c400, v3
	v_add_u32_e32 v153, 0x1c800, v3
	v_add_u32_e32 v154, 0x1cc00, v3
	v_add_u32_e32 v155, s8, v2
	v_mov_b32_e32 v156, 0x7f7f7f7f
	s_movk_i32 s65, 0x1c00
	s_mov_b32 s7, 0x3a800000
	s_mov_b32 s66, 0xc3e00000
	v_mov_b32_e32 v157, 0x43e00000
	s_mov_b64 s[16:17], s[24:25]
	s_mov_b64 s[14:15], s[22:23]
	s_barrier
	s_nop 0
	s_nop 0
	s_nop 0
	s_nop 0
	s_nop 0
	s_nop 0
	s_nop 0
	s_nop 0
	s_nop 0
	s_nop 0
	s_nop 0
	s_nop 0
	s_nop 0
	s_nop 0
	s_nop 0
